# GEMM1 and GEMM2 K-loops: removed the blanket lgkmcnt(0) after each barrier, MFMAs start on per-fragment waits
# baseline (speedup 1.0000x reference)
.LBB0_990:
	s_lshl_b32 s0, s64, 19
	s_and_b64 s[22:23], s[34:35], exec
	s_cselect_b32 s1, s0, s68
	s_add_i32 s18, s18, 0
	s_add_i32 s18, s18, 0x20000
	v_mov_b32_e32 v34, 0
	v_add3_u32 v180, s18, v171, v172
	v_add3_u32 v181, s18, v173, v174
	s_mov_b32 s70, -2
	s_movk_i32 s71, 0x100
	ds_read_b128 v[2:5], v176
	ds_read_b128 v[6:9], v176 offset:1024
	ds_read_b128 v[10:13], v176 offset:2048
	ds_read_b128 v[14:17], v176 offset:3072
	s_add_i32 s72, s68, s71
	s_cmp_eq_u32 s70, 12
	s_cselect_b64 s[22:23], -1, 0
	s_and_b64 s[18:19], s[22:23], exec
	s_cselect_b32 s72, s1, s72
	s_add_i32 s18, s71, 0xffffff80
	s_mov_b32 m0, s51
	ds_read_b128 v[182:185], v177
	ds_read_b128 v[186:189], v177 offset:1024
	ds_read_b128 v[190:193], v177 offset:2048
	ds_read_b128 v[194:197], v177 offset:3072
	ds_read_b128 v[198:201], v177 offset:4096
	ds_read_b128 v[202:205], v177 offset:5120
	ds_read_b128 v[206:209], v177 offset:6144
	ds_read_b128 v[210:213], v177 offset:7168
	buffer_load_dwordx4 v165, s[12:15], s18 offen lds
	s_mov_b32 m0, s52
	s_nop 0
	buffer_load_dwordx4 v169, s[12:15], s18 offen lds
	s_waitcnt lgkmcnt(8)
	s_barrier
	s_setprio 1
	s_waitcnt lgkmcnt(6)
	v_mfma_f32_16x16x128_f8f6f4 v[142:145], v[2:9], v[182:189], 0
	v_mfma_f32_16x16x128_f8f6f4 v[134:137], v[10:17], v[182:189], 0
	s_waitcnt lgkmcnt(4)
	v_mfma_f32_16x16x128_f8f6f4 v[126:129], v[2:9], v[190:197], 0
	v_mfma_f32_16x16x128_f8f6f4 v[118:121], v[10:17], v[190:197], 0
	s_waitcnt lgkmcnt(2)
	v_mfma_f32_16x16x128_f8f6f4 v[146:149], v[2:9], v[198:205], 0
	v_mfma_f32_16x16x128_f8f6f4 v[150:153], v[10:17], v[198:205], 0
	s_waitcnt lgkmcnt(0)
	v_mfma_f32_16x16x128_f8f6f4 v[154:157], v[2:9], v[206:213], 0
	v_mfma_f32_16x16x128_f8f6f4 v[158:161], v[10:17], v[206:213], 0
	s_setprio 0
	s_barrier
	s_mov_b32 s18, s14
	s_mov_b32 s19, s15
	s_mov_b32 m0, s33
	s_nop 1
	ds_read_b128 v[18:21], v178
	ds_read_b128 v[22:25], v178 offset:1024
	ds_read_b128 v[26:29], v178 offset:2048
	ds_read_b128 v[30:33], v178 offset:3072
	buffer_load_dwordx4 v166, s[16:19], s72 offen lds
	s_mov_b32 m0, s36
	s_nop 0
	buffer_load_dwordx4 v168, s[16:19], s72 offen lds
	s_barrier
	s_setprio 1
	s_waitcnt lgkmcnt(2)
	v_mfma_f32_16x16x128_f8f6f4 v[138:141], v[18:25], v[182:189], 0
	s_and_b64 s[74:75], s[34:35], s[22:23]
	s_waitcnt lgkmcnt(0)
	v_mfma_f32_16x16x128_f8f6f4 v[130:133], v[26:33], v[182:189], 0
	v_mfma_f32_16x16x128_f8f6f4 v[122:125], v[18:25], v[190:197], 0
	v_mfma_f32_16x16x128_f8f6f4 v[114:117], v[26:33], v[190:197], 0
	v_mfma_f32_16x16x128_f8f6f4 v[110:113], v[18:25], v[198:205], 0
	v_mfma_f32_16x16x128_f8f6f4 v[106:109], v[26:33], v[198:205], 0
	v_mfma_f32_16x16x128_f8f6f4 v[102:105], v[18:25], v[206:213], 0
	v_mfma_f32_16x16x128_f8f6f4 v[98:101], v[26:33], v[206:213], 0
	s_setprio 0
	s_andn2_b64 vcc, exec, s[74:75]
	s_barrier
	s_or_b32 s73, s72, 0x80
	s_and_b64 s[22:23], s[22:23], exec
	s_mov_b32 m0, s29
	s_cselect_b32 s22, 0, s71
	ds_read_b128 v[182:185], v177 offset:16384
	ds_read_b128 v[186:189], v177 offset:17408
	ds_read_b128 v[190:193], v177 offset:18432
	ds_read_b128 v[194:197], v177 offset:19456
	ds_read_b128 v[198:201], v177 offset:20480
	ds_read_b128 v[202:205], v177 offset:21504
	ds_read_b128 v[206:209], v177 offset:22528
	ds_read_b128 v[210:213], v177 offset:23552
	buffer_load_dwordx4 v164, s[12:15], s22 offen lds
	s_mov_b32 m0, s37
	s_or_b32 s23, s22, 0x80
	buffer_load_dwordx4 v167, s[12:15], s22 offen lds
	s_barrier
	s_setprio 1
	s_waitcnt lgkmcnt(6)
	v_mfma_f32_16x16x128_f8f6f4 v[94:97], v[2:9], v[182:189], 0
	v_mfma_f32_16x16x128_f8f6f4 v[86:89], v[10:17], v[182:189], 0
	s_waitcnt lgkmcnt(4)
	v_mfma_f32_16x16x128_f8f6f4 v[78:81], v[2:9], v[190:197], 0
	v_mfma_f32_16x16x128_f8f6f4 v[70:73], v[10:17], v[190:197], 0
	s_waitcnt lgkmcnt(2)
	v_mfma_f32_16x16x128_f8f6f4 v[214:217], v[2:9], v[198:205], 0
	v_mfma_f32_16x16x128_f8f6f4 v[218:221], v[10:17], v[198:205], 0
	s_waitcnt lgkmcnt(0)
	v_mfma_f32_16x16x128_f8f6f4 v[222:225], v[2:9], v[206:213], 0
	v_mfma_f32_16x16x128_f8f6f4 v[226:229], v[10:17], v[206:213], 0
	s_setprio 0
	s_barrier
	s_add_i32 s74, s72, 0x40000
	s_mov_b32 m0, s38
	s_nop 0
	buffer_load_dwordx4 v166, s[16:19], s74 offen lds
	s_mov_b32 m0, s39
	s_nop 0
	buffer_load_dwordx4 v168, s[16:19], s74 offen lds
	s_waitcnt vmcnt(6)
	s_barrier
	s_setprio 1
	v_mfma_f32_16x16x128_f8f6f4 v[90:93], v[18:25], v[182:189], 0
	v_mfma_f32_16x16x128_f8f6f4 v[82:85], v[26:33], v[182:189], 0
	v_mfma_f32_16x16x128_f8f6f4 v[74:77], v[18:25], v[190:197], 0
	v_mfma_f32_16x16x128_f8f6f4 v[66:69], v[26:33], v[190:197], 0
	v_mfma_f32_16x16x128_f8f6f4 v[230:233], v[18:25], v[198:205], 0
	v_mfma_f32_16x16x128_f8f6f4 v[234:237], v[26:33], v[198:205], 0
	v_mfma_f32_16x16x128_f8f6f4 v[238:241], v[18:25], v[206:213], 0
	v_mfma_f32_16x16x128_f8f6f4 v[242:245], v[26:33], v[206:213], 0
	s_setprio 0
	v_add_u32_e32 v14, 0x18000, v175
	s_barrier
	s_branch .Lmid_g1
.LBB0_991:
	s_or_b32 s73, s72, 0x80
	s_and_b64 s[22:23], s[22:23], exec
	s_mov_b32 m0, s29
	s_cselect_b32 s22, 0, s71
	ds_read_b128 v[182:185], v177 offset:16384
	ds_read_b128 v[186:189], v177 offset:17408
	ds_read_b128 v[190:193], v177 offset:18432
	ds_read_b128 v[194:197], v177 offset:19456
	ds_read_b128 v[198:201], v177 offset:20480
	ds_read_b128 v[202:205], v177 offset:21504
	ds_read_b128 v[206:209], v177 offset:22528
	ds_read_b128 v[210:213], v177 offset:23552
	buffer_load_dwordx4 v164, s[12:15], s22 offen lds
	s_mov_b32 m0, s37
	s_or_b32 s23, s22, 0x80
	buffer_load_dwordx4 v167, s[12:15], s22 offen lds
	s_barrier
	s_setprio 1
	s_waitcnt lgkmcnt(6)
	v_mfma_f32_16x16x128_f8f6f4 v[94:97], v[2:9], v[182:189], v[94:97]
	v_mfma_f32_16x16x128_f8f6f4 v[86:89], v[10:17], v[182:189], v[86:89]
	s_waitcnt lgkmcnt(4)
	v_mfma_f32_16x16x128_f8f6f4 v[78:81], v[2:9], v[190:197], v[78:81]
	v_mfma_f32_16x16x128_f8f6f4 v[70:73], v[10:17], v[190:197], v[70:73]
	s_waitcnt lgkmcnt(2)
	v_mfma_f32_16x16x128_f8f6f4 v[214:217], v[2:9], v[198:205], v[62:65]
	v_mfma_f32_16x16x128_f8f6f4 v[218:221], v[10:17], v[198:205], v[54:57]
	s_waitcnt lgkmcnt(0)
	v_mfma_f32_16x16x128_f8f6f4 v[222:225], v[2:9], v[206:213], v[46:49]
	v_mfma_f32_16x16x128_f8f6f4 v[226:229], v[10:17], v[206:213], v[38:41]
	s_setprio 0
	s_barrier
	s_add_i32 s74, s72, 0x40000
	s_mov_b32 m0, s38
	s_nop 0
	buffer_load_dwordx4 v166, s[16:19], s74 offen lds
	s_mov_b32 m0, s39
	s_nop 0
	buffer_load_dwordx4 v168, s[16:19], s74 offen lds
	s_waitcnt vmcnt(6)
	s_barrier
	s_setprio 1
	v_mfma_f32_16x16x128_f8f6f4 v[90:93], v[18:25], v[182:189], v[90:93]
	v_mfma_f32_16x16x128_f8f6f4 v[82:85], v[26:33], v[182:189], v[82:85]
	v_mfma_f32_16x16x128_f8f6f4 v[74:77], v[18:25], v[190:197], v[74:77]
	v_mfma_f32_16x16x128_f8f6f4 v[66:69], v[26:33], v[190:197], v[66:69]
	v_mfma_f32_16x16x128_f8f6f4 v[230:233], v[18:25], v[198:205], v[58:61]
	v_mfma_f32_16x16x128_f8f6f4 v[234:237], v[26:33], v[198:205], v[50:53]
	v_mfma_f32_16x16x128_f8f6f4 v[238:241], v[18:25], v[206:213], v[42:45]
	v_mfma_f32_16x16x128_f8f6f4 v[242:245], v[26:33], v[206:213], v[34:37]
	s_setprio 0
	v_add_u32_e32 v14, 0x18000, v175
	s_barrier
.Lmid_g1:
	ds_read_b128 v[2:5], v14
	ds_read_b128 v[6:9], v14 offset:1024
	ds_read_b128 v[10:13], v14 offset:2048
	ds_read_b128 v[14:17], v14 offset:3072
	s_mov_b32 m0, s40
	ds_read_b128 v[34:37], v177 offset:32768
	ds_read_b128 v[38:41], v177 offset:33792
	ds_read_b128 v[42:45], v177 offset:34816
	ds_read_b128 v[46:49], v177 offset:35840
	ds_read_b128 v[50:53], v177 offset:36864
	ds_read_b128 v[54:57], v177 offset:37888
	ds_read_b128 v[58:61], v177 offset:38912
	ds_read_b128 v[62:65], v177 offset:39936
	buffer_load_dwordx4 v165, s[12:15], s22 offen lds
	s_mov_b32 m0, s41
	s_nop 0
	buffer_load_dwordx4 v169, s[12:15], s22 offen lds
	s_waitcnt lgkmcnt(8)
	s_barrier
	s_setprio 1
	s_waitcnt lgkmcnt(6)
	v_mfma_f32_16x16x128_f8f6f4 v[142:145], v[2:9], v[34:41], v[142:145]
	v_mfma_f32_16x16x128_f8f6f4 v[134:137], v[10:17], v[34:41], v[134:137]
	s_waitcnt lgkmcnt(4)
	v_mfma_f32_16x16x128_f8f6f4 v[126:129], v[2:9], v[42:49], v[126:129]
	v_mfma_f32_16x16x128_f8f6f4 v[118:121], v[10:17], v[42:49], v[118:121]
	s_waitcnt lgkmcnt(2)
	v_mfma_f32_16x16x128_f8f6f4 v[30:33], v[2:9], v[50:57], v[146:149]
	v_mfma_f32_16x16x128_f8f6f4 v[26:29], v[10:17], v[50:57], v[150:153]
	s_waitcnt lgkmcnt(0)
	v_mfma_f32_16x16x128_f8f6f4 v[22:25], v[2:9], v[58:65], v[154:157]
	v_mfma_f32_16x16x128_f8f6f4 v[18:21], v[10:17], v[58:65], v[158:161]
	s_setprio 0
	s_barrier
	s_nop 4
	v_add_u32_e32 v158, 0x1c000, v175
	s_mov_b32 m0, s45
	ds_read_b128 v[146:149], v158
	ds_read_b128 v[150:153], v158 offset:1024
	ds_read_b128 v[154:157], v158 offset:2048
	ds_read_b128 v[158:161], v158 offset:3072
	buffer_load_dwordx4 v166, s[16:19], s73 offen lds
	s_mov_b32 m0, s46
	s_nop 0
	buffer_load_dwordx4 v168, s[16:19], s73 offen lds
	s_barrier
	s_setprio 1
	s_waitcnt lgkmcnt(2)
	v_mfma_f32_16x16x128_f8f6f4 v[138:141], v[146:153], v[34:41], v[138:141]
	s_waitcnt lgkmcnt(0)
	v_mfma_f32_16x16x128_f8f6f4 v[130:133], v[154:161], v[34:41], v[130:133]
	v_mfma_f32_16x16x128_f8f6f4 v[122:125], v[146:153], v[42:49], v[122:125]
	v_mfma_f32_16x16x128_f8f6f4 v[114:117], v[154:161], v[42:49], v[114:117]
	v_mfma_f32_16x16x128_f8f6f4 v[110:113], v[146:153], v[50:57], v[110:113]
	v_mfma_f32_16x16x128_f8f6f4 v[106:109], v[154:161], v[50:57], v[106:109]
	v_mfma_f32_16x16x128_f8f6f4 v[102:105], v[146:153], v[58:65], v[102:105]
	v_mfma_f32_16x16x128_f8f6f4 v[98:101], v[154:161], v[58:65], v[98:101]
	s_setprio 0
	s_mov_b32 m0, s47
	s_barrier
	ds_read_b128 v[182:185], v177 offset:49152
	ds_read_b128 v[186:189], v177 offset:50176
	ds_read_b128 v[190:193], v177 offset:51200
	ds_read_b128 v[194:197], v177 offset:52224
	ds_read_b128 v[198:201], v177 offset:53248
	ds_read_b128 v[202:205], v177 offset:54272
	ds_read_b128 v[206:209], v177 offset:55296
	ds_read_b128 v[210:213], v177 offset:56320
	buffer_load_dwordx4 v164, s[12:15], s23 offen lds
	s_mov_b32 m0, s48
	s_nop 0
	buffer_load_dwordx4 v167, s[12:15], s23 offen lds
	s_barrier
	s_setprio 1
	s_waitcnt lgkmcnt(6)
	v_mfma_f32_16x16x128_f8f6f4 v[94:97], v[2:9], v[182:189], v[94:97]
	v_mfma_f32_16x16x128_f8f6f4 v[86:89], v[10:17], v[182:189], v[86:89]
	s_waitcnt lgkmcnt(4)
	v_mfma_f32_16x16x128_f8f6f4 v[78:81], v[2:9], v[190:197], v[78:81]
	v_mfma_f32_16x16x128_f8f6f4 v[70:73], v[10:17], v[190:197], v[70:73]
	s_waitcnt lgkmcnt(2)
	v_mfma_f32_16x16x128_f8f6f4 v[62:65], v[2:9], v[198:205], v[214:217]
	v_mfma_f32_16x16x128_f8f6f4 v[54:57], v[10:17], v[198:205], v[218:221]
	s_waitcnt lgkmcnt(0)
	v_mfma_f32_16x16x128_f8f6f4 v[46:49], v[2:9], v[206:213], v[222:225]
	v_mfma_f32_16x16x128_f8f6f4 v[38:41], v[10:17], v[206:213], v[226:229]
	s_setprio 0
	s_barrier
	s_add_i32 s72, s72, 0x40080
	s_mov_b32 m0, s49
	s_nop 0
	buffer_load_dwordx4 v166, s[16:19], s72 offen lds
	s_mov_b32 m0, s50
	s_nop 0
	buffer_load_dwordx4 v168, s[16:19], s72 offen lds
	s_waitcnt vmcnt(6)
	s_barrier
	s_setprio 1
	v_mfma_f32_16x16x128_f8f6f4 v[90:93], v[146:153], v[182:189], v[90:93]
	v_mfma_f32_16x16x128_f8f6f4 v[82:85], v[154:161], v[182:189], v[82:85]
	v_mfma_f32_16x16x128_f8f6f4 v[74:77], v[146:153], v[190:197], v[74:77]
	v_mfma_f32_16x16x128_f8f6f4 v[66:69], v[154:161], v[190:197], v[66:69]
	v_mfma_f32_16x16x128_f8f6f4 v[58:61], v[146:153], v[198:205], v[230:233]
	v_mfma_f32_16x16x128_f8f6f4 v[50:53], v[154:161], v[198:205], v[234:237]
	v_mfma_f32_16x16x128_f8f6f4 v[42:45], v[146:153], v[206:213], v[238:241]
	v_mfma_f32_16x16x128_f8f6f4 v[34:37], v[154:161], v[206:213], v[242:245]
	s_setprio 0
	s_add_i32 s70, s70, 2
	s_addk_i32 s71, 0x100
	s_cmp_gt_u32 s70, 13
	s_barrier
	s_cbranch_scc1 .LBB0_979
.LBB0_992:
	ds_read_b128 v[2:5], v176
	ds_read_b128 v[6:9], v176 offset:1024
	ds_read_b128 v[10:13], v176 offset:2048
	ds_read_b128 v[14:17], v176 offset:3072
	s_add_i32 s72, s68, s71
	s_cmp_eq_u32 s70, 12
	s_cselect_b64 s[22:23], -1, 0
	s_and_b64 s[18:19], s[22:23], exec
	s_cselect_b32 s72, s1, s72
	s_add_i32 s18, s71, 0xffffff80
	s_mov_b32 m0, s51
	ds_read_b128 v[182:185], v177
	ds_read_b128 v[186:189], v177 offset:1024
	ds_read_b128 v[190:193], v177 offset:2048
	ds_read_b128 v[194:197], v177 offset:3072
	ds_read_b128 v[198:201], v177 offset:4096
	ds_read_b128 v[202:205], v177 offset:5120
	ds_read_b128 v[206:209], v177 offset:6144
	ds_read_b128 v[210:213], v177 offset:7168
	buffer_load_dwordx4 v165, s[12:15], s18 offen lds
	s_mov_b32 m0, s52
	s_nop 0
	buffer_load_dwordx4 v169, s[12:15], s18 offen lds
	s_waitcnt lgkmcnt(8)
	s_barrier
	s_setprio 1
	s_waitcnt lgkmcnt(6)
	v_mfma_f32_16x16x128_f8f6f4 v[142:145], v[2:9], v[182:189], v[142:145]
	v_mfma_f32_16x16x128_f8f6f4 v[134:137], v[10:17], v[182:189], v[134:137]
	s_waitcnt lgkmcnt(4)
	v_mfma_f32_16x16x128_f8f6f4 v[126:129], v[2:9], v[190:197], v[126:129]
	v_mfma_f32_16x16x128_f8f6f4 v[118:121], v[10:17], v[190:197], v[118:121]
	s_waitcnt lgkmcnt(2)
	v_mfma_f32_16x16x128_f8f6f4 v[146:149], v[2:9], v[198:205], v[30:33]
	v_mfma_f32_16x16x128_f8f6f4 v[150:153], v[10:17], v[198:205], v[26:29]
	s_waitcnt lgkmcnt(0)
	v_mfma_f32_16x16x128_f8f6f4 v[154:157], v[2:9], v[206:213], v[22:25]
	v_mfma_f32_16x16x128_f8f6f4 v[158:161], v[10:17], v[206:213], v[18:21]
	s_setprio 0
	s_barrier
	s_mov_b32 s18, s14
	s_mov_b32 s19, s15
	s_mov_b32 m0, s33
	s_nop 1
	ds_read_b128 v[18:21], v178
	ds_read_b128 v[22:25], v178 offset:1024
	ds_read_b128 v[26:29], v178 offset:2048
	ds_read_b128 v[30:33], v178 offset:3072
	buffer_load_dwordx4 v166, s[16:19], s72 offen lds
	s_mov_b32 m0, s36
	s_nop 0
	buffer_load_dwordx4 v168, s[16:19], s72 offen lds
	s_barrier
	s_setprio 1
	s_waitcnt lgkmcnt(2)
	v_mfma_f32_16x16x128_f8f6f4 v[138:141], v[18:25], v[182:189], v[138:141]
	s_and_b64 s[74:75], s[34:35], s[22:23]
	s_waitcnt lgkmcnt(0)
	v_mfma_f32_16x16x128_f8f6f4 v[130:133], v[26:33], v[182:189], v[130:133]
	v_mfma_f32_16x16x128_f8f6f4 v[122:125], v[18:25], v[190:197], v[122:125]
	v_mfma_f32_16x16x128_f8f6f4 v[114:117], v[26:33], v[190:197], v[114:117]
	v_mfma_f32_16x16x128_f8f6f4 v[110:113], v[18:25], v[198:205], v[110:113]
	v_mfma_f32_16x16x128_f8f6f4 v[106:109], v[26:33], v[198:205], v[106:109]
	v_mfma_f32_16x16x128_f8f6f4 v[102:105], v[18:25], v[206:213], v[102:105]
	v_mfma_f32_16x16x128_f8f6f4 v[98:101], v[26:33], v[206:213], v[98:101]
	s_setprio 0
	s_andn2_b64 vcc, exec, s[74:75]
	s_barrier
	s_cbranch_vccnz .LBB0_991
	ds_read2st64_b32 v[164:165], v180 offset1:2
	ds_read2st64_b32 v[182:183], v181 offset1:2
	s_waitcnt lgkmcnt(0)
	s_waitcnt lgkmcnt(1)
	v_lshlrev_b32_e32 v164, 9, v164
	v_lshlrev_b32_e32 v165, 9, v165
	s_waitcnt lgkmcnt(0)
	v_lshlrev_b32_e32 v167, 9, v182
	v_lshlrev_b32_e32 v169, 9, v183
	v_and_b32_e32 v164, 0xfffff800, v164
	v_and_b32_e32 v165, 0xfffff800, v165
	v_and_b32_e32 v167, 0xfffff800, v167
	v_and_b32_e32 v169, 0xfffff800, v169
	v_add_u32_e32 v164, v164, v162
	v_add_u32_e32 v165, v165, v162
	v_add_u32_e32 v167, v167, v163
	v_add_u32_e32 v169, v169, v163
	s_branch .LBB0_991

.LBB0_1080:
	s_lshl_b32 s10, s60, 19
	s_and_b64 s[18:19], s[0:1], exec
	s_cselect_b32 s18, s10, s67
	s_lshl_b32 s11, s62, 19
	s_and_b64 s[0:1], s[0:1], exec
	v_mov_b32_e32 v26, 0
	s_cselect_b32 s0, s11, s66
	s_add_i32 s1, s67, 0x40080
	s_add_i32 s19, s66, 0x100
	s_mov_b32 s66, -2
	s_waitcnt lgkmcnt(0)
	ds_read_b128 v[126:129], v153
	ds_read_b128 v[130:133], v153 offset:1024
	ds_read_b128 v[138:141], v153 offset:2048
	ds_read_b128 v[142:145], v153 offset:3072
	s_add_i32 s26, s1, 0xfffc0080
	s_cmp_eq_u32 s66, 12
	s_cselect_b32 s69, s18, s26
	s_cselect_b32 s67, s0, s19
	s_or_b32 s68, s69, 0x80
	s_mov_b32 m0, s51
	ds_read_b128 v[160:163], v154
	ds_read_b128 v[164:167], v154 offset:1024
	ds_read_b128 v[168:171], v154 offset:2048
	ds_read_b128 v[172:175], v154 offset:3072
	ds_read_b128 v[176:179], v154 offset:4096
	ds_read_b128 v[180:183], v154 offset:5120
	ds_read_b128 v[184:187], v154 offset:6144
	ds_read_b128 v[188:191], v154 offset:7168
	buffer_load_dwordx4 v1, s[20:23], s1 offen lds
	s_mov_b32 m0, s52
	s_nop 0
	buffer_load_dwordx4 v252, s[20:23], s1 offen lds
	s_waitcnt lgkmcnt(8)
	s_barrier
	s_setprio 1
	s_waitcnt lgkmcnt(6)
	v_mfma_f32_16x16x128_f8f6f4 v[134:137], v[126:133], v[160:167], 0
	v_mfma_f32_16x16x128_f8f6f4 v[122:125], v[138:145], v[160:167], 0
	s_waitcnt lgkmcnt(4)
	v_mfma_f32_16x16x128_f8f6f4 v[192:195], v[126:133], v[168:175], 0
	v_mfma_f32_16x16x128_f8f6f4 v[196:199], v[138:145], v[168:175], 0
	s_waitcnt lgkmcnt(2)
	v_mfma_f32_16x16x128_f8f6f4 v[200:203], v[126:133], v[176:183], 0
	v_mfma_f32_16x16x128_f8f6f4 v[204:207], v[138:145], v[176:183], 0
	s_waitcnt lgkmcnt(0)
	v_mfma_f32_16x16x128_f8f6f4 v[208:211], v[126:133], v[184:191], 0
	v_mfma_f32_16x16x128_f8f6f4 v[212:215], v[138:145], v[184:191], 0
	s_setprio 0
	s_barrier
	s_mov_b32 s26, s22
	s_mov_b32 s27, s23
	s_mov_b32 m0, s36
	s_nop 1
	ds_read_b128 v[74:77], v155
	ds_read_b128 v[78:81], v155 offset:1024
	ds_read_b128 v[90:93], v155 offset:2048
	ds_read_b128 v[94:97], v155 offset:3072
	buffer_load_dwordx4 v253, s[24:27], s67 offen lds
	s_mov_b32 m0, s37
	s_nop 0
	buffer_load_dwordx4 v150, s[24:27], s67 offen lds
	s_barrier
	s_setprio 1
	s_waitcnt lgkmcnt(2)
	v_mfma_f32_16x16x128_f8f6f4 v[118:121], v[74:81], v[160:167], 0
	s_waitcnt lgkmcnt(0)
	v_mfma_f32_16x16x128_f8f6f4 v[114:117], v[90:97], v[160:167], 0
	v_mfma_f32_16x16x128_f8f6f4 v[160:163], v[74:81], v[168:175], 0
	v_mfma_f32_16x16x128_f8f6f4 v[164:167], v[90:97], v[168:175], 0
	v_mfma_f32_16x16x128_f8f6f4 v[168:171], v[74:81], v[176:183], 0
	v_mfma_f32_16x16x128_f8f6f4 v[172:175], v[90:97], v[176:183], 0
	v_mfma_f32_16x16x128_f8f6f4 v[176:179], v[74:81], v[184:191], 0
	v_mfma_f32_16x16x128_f8f6f4 v[180:183], v[90:97], v[184:191], 0
	s_setprio 0
	s_mov_b32 m0, s35
	s_barrier
	s_nop 3
	ds_read_b128 v[66:69], v154 offset:16384
	ds_read_b128 v[70:73], v154 offset:17408
	ds_read_b128 v[82:85], v154 offset:18432
	ds_read_b128 v[86:89], v154 offset:19456
	ds_read_b128 v[98:101], v154 offset:20480
	ds_read_b128 v[102:105], v154 offset:21504
	ds_read_b128 v[106:109], v154 offset:22528
	ds_read_b128 v[110:113], v154 offset:23552
	buffer_load_dwordx4 v1, s[20:23], s69 offen lds
	s_mov_b32 m0, s38
	s_nop 0
	buffer_load_dwordx4 v252, s[20:23], s69 offen lds
	s_barrier
	s_setprio 1
	s_waitcnt lgkmcnt(6)
	v_mfma_f32_16x16x128_f8f6f4 v[62:65], v[126:133], v[66:73], 0
	v_mfma_f32_16x16x128_f8f6f4 v[58:61], v[138:145], v[66:73], 0
	s_waitcnt lgkmcnt(4)
	v_mfma_f32_16x16x128_f8f6f4 v[184:187], v[126:133], v[82:89], 0
	v_mfma_f32_16x16x128_f8f6f4 v[188:191], v[138:145], v[82:89], 0
	s_waitcnt lgkmcnt(2)
	v_mfma_f32_16x16x128_f8f6f4 v[216:219], v[126:133], v[98:105], 0
	v_mfma_f32_16x16x128_f8f6f4 v[220:223], v[138:145], v[98:105], 0
	s_waitcnt lgkmcnt(0)
	v_mfma_f32_16x16x128_f8f6f4 v[224:227], v[126:133], v[106:113], 0
	v_mfma_f32_16x16x128_f8f6f4 v[228:231], v[138:145], v[106:113], 0
	s_setprio 0
	s_barrier
	s_add_i32 s70, s67, 0x40000
	s_mov_b32 m0, s39
	s_nop 0
	buffer_load_dwordx4 v253, s[24:27], s70 offen lds
	s_mov_b32 m0, s40
	s_nop 0
	buffer_load_dwordx4 v150, s[24:27], s70 offen lds
	s_waitcnt vmcnt(6)
	s_barrier
	s_setprio 1
	v_mfma_f32_16x16x128_f8f6f4 v[54:57], v[74:81], v[66:73], 0
	v_mfma_f32_16x16x128_f8f6f4 v[50:53], v[90:97], v[66:73], 0
	v_mfma_f32_16x16x128_f8f6f4 v[232:235], v[74:81], v[82:89], 0
	v_mfma_f32_16x16x128_f8f6f4 v[236:239], v[90:97], v[82:89], 0
	v_mfma_f32_16x16x128_f8f6f4 v[240:243], v[74:81], v[98:105], 0
	v_mfma_f32_16x16x128_f8f6f4 v[244:247], v[90:97], v[98:105], 0
	v_mfma_f32_16x16x128_f8f6f4 v[248:251], v[74:81], v[106:113], 0
	v_mfma_f32_16x16x128_f8f6f4 v[146:149], v[90:97], v[106:113], 0
	s_setprio 0
	s_barrier
	s_branch .Lmid_g2
.LBB0_1081:
	s_waitcnt lgkmcnt(0)
	ds_read_b128 v[126:129], v153
	ds_read_b128 v[130:133], v153 offset:1024
	ds_read_b128 v[138:141], v153 offset:2048
	ds_read_b128 v[142:145], v153 offset:3072
	s_add_i32 s26, s1, 0xfffc0080
	s_cmp_eq_u32 s66, 12
	s_cselect_b32 s69, s18, s26
	s_cselect_b32 s67, s0, s19
	s_or_b32 s68, s69, 0x80
	s_mov_b32 m0, s51
	ds_read_b128 v[160:163], v154
	ds_read_b128 v[164:167], v154 offset:1024
	ds_read_b128 v[168:171], v154 offset:2048
	ds_read_b128 v[172:175], v154 offset:3072
	ds_read_b128 v[176:179], v154 offset:4096
	ds_read_b128 v[180:183], v154 offset:5120
	ds_read_b128 v[184:187], v154 offset:6144
	ds_read_b128 v[188:191], v154 offset:7168
	buffer_load_dwordx4 v1, s[20:23], s1 offen lds
	s_mov_b32 m0, s52
	s_nop 0
	buffer_load_dwordx4 v252, s[20:23], s1 offen lds
	s_waitcnt lgkmcnt(8)
	s_barrier
	s_setprio 1
	s_waitcnt lgkmcnt(6)
	v_mfma_f32_16x16x128_f8f6f4 v[134:137], v[126:133], v[160:167], v[134:137]
	v_mfma_f32_16x16x128_f8f6f4 v[122:125], v[138:145], v[160:167], v[122:125]
	s_waitcnt lgkmcnt(4)
	v_mfma_f32_16x16x128_f8f6f4 v[192:195], v[126:133], v[168:175], v[110:113]
	v_mfma_f32_16x16x128_f8f6f4 v[196:199], v[138:145], v[168:175], v[106:109]
	s_waitcnt lgkmcnt(2)
	v_mfma_f32_16x16x128_f8f6f4 v[200:203], v[126:133], v[176:183], v[94:97]
	v_mfma_f32_16x16x128_f8f6f4 v[204:207], v[138:145], v[176:183], v[90:93]
	s_waitcnt lgkmcnt(0)
	v_mfma_f32_16x16x128_f8f6f4 v[208:211], v[126:133], v[184:191], v[78:81]
	v_mfma_f32_16x16x128_f8f6f4 v[212:215], v[138:145], v[184:191], v[74:77]
	s_setprio 0
	s_barrier
	s_mov_b32 s26, s22
	s_mov_b32 s27, s23
	s_mov_b32 m0, s36
	s_nop 1
	ds_read_b128 v[74:77], v155
	ds_read_b128 v[78:81], v155 offset:1024
	ds_read_b128 v[90:93], v155 offset:2048
	ds_read_b128 v[94:97], v155 offset:3072
	buffer_load_dwordx4 v253, s[24:27], s67 offen lds
	s_mov_b32 m0, s37
	s_nop 0
	buffer_load_dwordx4 v150, s[24:27], s67 offen lds
	s_barrier
	s_setprio 1
	s_waitcnt lgkmcnt(2)
	v_mfma_f32_16x16x128_f8f6f4 v[118:121], v[74:81], v[160:167], v[118:121]
	s_waitcnt lgkmcnt(0)
	v_mfma_f32_16x16x128_f8f6f4 v[114:117], v[90:97], v[160:167], v[114:117]
	v_mfma_f32_16x16x128_f8f6f4 v[160:163], v[74:81], v[168:175], v[102:105]
	v_mfma_f32_16x16x128_f8f6f4 v[164:167], v[90:97], v[168:175], v[98:101]
	v_mfma_f32_16x16x128_f8f6f4 v[168:171], v[74:81], v[176:183], v[86:89]
	v_mfma_f32_16x16x128_f8f6f4 v[172:175], v[90:97], v[176:183], v[82:85]
	v_mfma_f32_16x16x128_f8f6f4 v[176:179], v[74:81], v[184:191], v[70:73]
	v_mfma_f32_16x16x128_f8f6f4 v[180:183], v[90:97], v[184:191], v[66:69]
	s_setprio 0
	s_mov_b32 m0, s35
	s_barrier
	s_nop 3
	ds_read_b128 v[66:69], v154 offset:16384
	ds_read_b128 v[70:73], v154 offset:17408
	ds_read_b128 v[82:85], v154 offset:18432
	ds_read_b128 v[86:89], v154 offset:19456
	ds_read_b128 v[98:101], v154 offset:20480
	ds_read_b128 v[102:105], v154 offset:21504
	ds_read_b128 v[106:109], v154 offset:22528
	ds_read_b128 v[110:113], v154 offset:23552
	buffer_load_dwordx4 v1, s[20:23], s69 offen lds
	s_mov_b32 m0, s38
	s_nop 0
	buffer_load_dwordx4 v252, s[20:23], s69 offen lds
	s_barrier
	s_setprio 1
	s_waitcnt lgkmcnt(6)
	v_mfma_f32_16x16x128_f8f6f4 v[62:65], v[126:133], v[66:73], v[62:65]
	v_mfma_f32_16x16x128_f8f6f4 v[58:61], v[138:145], v[66:73], v[58:61]
	s_waitcnt lgkmcnt(4)
	v_mfma_f32_16x16x128_f8f6f4 v[184:187], v[126:133], v[82:89], v[46:49]
	v_mfma_f32_16x16x128_f8f6f4 v[188:191], v[138:145], v[82:89], v[42:45]
	s_waitcnt lgkmcnt(2)
	v_mfma_f32_16x16x128_f8f6f4 v[216:219], v[126:133], v[98:105], v[22:25]
	v_mfma_f32_16x16x128_f8f6f4 v[220:223], v[138:145], v[98:105], v[18:21]
	s_waitcnt lgkmcnt(0)
	v_mfma_f32_16x16x128_f8f6f4 v[224:227], v[126:133], v[106:113], v[6:9]
	v_mfma_f32_16x16x128_f8f6f4 v[228:231], v[138:145], v[106:113], v[2:5]
	s_setprio 0
	s_barrier
	s_add_i32 s70, s67, 0x40000
	s_mov_b32 m0, s39
	s_nop 0
	buffer_load_dwordx4 v253, s[24:27], s70 offen lds
	s_mov_b32 m0, s40
	s_nop 0
	buffer_load_dwordx4 v150, s[24:27], s70 offen lds
	s_waitcnt vmcnt(6)
	s_barrier
	s_setprio 1
	v_mfma_f32_16x16x128_f8f6f4 v[54:57], v[74:81], v[66:73], v[54:57]
	v_mfma_f32_16x16x128_f8f6f4 v[50:53], v[90:97], v[66:73], v[50:53]
	v_mfma_f32_16x16x128_f8f6f4 v[232:235], v[74:81], v[82:89], v[30:33]
	v_mfma_f32_16x16x128_f8f6f4 v[236:239], v[90:97], v[82:89], v[26:29]
	v_mfma_f32_16x16x128_f8f6f4 v[240:243], v[74:81], v[98:105], v[38:41]
	v_mfma_f32_16x16x128_f8f6f4 v[244:247], v[90:97], v[98:105], v[34:37]
	v_mfma_f32_16x16x128_f8f6f4 v[248:251], v[74:81], v[106:113], v[14:17]
	v_mfma_f32_16x16x128_f8f6f4 v[146:149], v[90:97], v[106:113], v[10:13]
	s_setprio 0
	s_barrier
.Lmid_g2:
	ds_read_b128 v[2:5], v156
	ds_read_b128 v[6:9], v156 offset:1024
	s_nop 2
	ds_read_b128 v[10:13], v156 offset:2048
	ds_read_b128 v[14:17], v156 offset:3072
	s_add_i32 s69, s69, 0x40000
	s_mov_b32 m0, s41
	ds_read_b128 v[18:21], v154 offset:32768
	ds_read_b128 v[22:25], v154 offset:33792
	ds_read_b128 v[26:29], v154 offset:34816
	ds_read_b128 v[30:33], v154 offset:35840
	ds_read_b128 v[34:37], v154 offset:36864
	ds_read_b128 v[38:41], v154 offset:37888
	ds_read_b128 v[42:45], v154 offset:38912
	ds_read_b128 v[46:49], v154 offset:39936
	buffer_load_dwordx4 v1, s[20:23], s69 offen lds
	s_mov_b32 m0, s42
	s_nop 0
	buffer_load_dwordx4 v252, s[20:23], s69 offen lds
	s_waitcnt lgkmcnt(8)
	s_barrier
	s_setprio 1
	s_waitcnt lgkmcnt(6)
	v_mfma_f32_16x16x128_f8f6f4 v[134:137], v[2:9], v[18:25], v[134:137]
	v_mfma_f32_16x16x128_f8f6f4 v[122:125], v[10:17], v[18:25], v[122:125]
	s_waitcnt lgkmcnt(4)
	v_mfma_f32_16x16x128_f8f6f4 v[110:113], v[2:9], v[26:33], v[192:195]
	v_mfma_f32_16x16x128_f8f6f4 v[106:109], v[10:17], v[26:33], v[196:199]
	s_waitcnt lgkmcnt(2)
	v_mfma_f32_16x16x128_f8f6f4 v[94:97], v[2:9], v[34:41], v[200:203]
	v_mfma_f32_16x16x128_f8f6f4 v[90:93], v[10:17], v[34:41], v[204:207]
	s_waitcnt lgkmcnt(0)
	v_mfma_f32_16x16x128_f8f6f4 v[78:81], v[2:9], v[42:49], v[208:211]
	v_mfma_f32_16x16x128_f8f6f4 v[74:77], v[10:17], v[42:49], v[212:215]
	s_setprio 0
	s_barrier
	s_add_i32 s69, s67, 0x80
	s_mov_b32 m0, s45
	ds_read_b128 v[126:129], v157
	ds_read_b128 v[130:133], v157 offset:1024
	ds_read_b128 v[138:141], v157 offset:2048
	ds_read_b128 v[142:145], v157 offset:3072
	buffer_load_dwordx4 v253, s[24:27], s69 offen lds
	s_mov_b32 m0, s46
	s_nop 0
	buffer_load_dwordx4 v150, s[24:27], s69 offen lds
	s_barrier
	s_setprio 1
	s_waitcnt lgkmcnt(2)
	v_mfma_f32_16x16x128_f8f6f4 v[118:121], v[126:133], v[18:25], v[118:121]
	s_waitcnt lgkmcnt(0)
	v_mfma_f32_16x16x128_f8f6f4 v[114:117], v[138:145], v[18:25], v[114:117]
	v_mfma_f32_16x16x128_f8f6f4 v[102:105], v[126:133], v[26:33], v[160:163]
	v_mfma_f32_16x16x128_f8f6f4 v[98:101], v[138:145], v[26:33], v[164:167]
	v_mfma_f32_16x16x128_f8f6f4 v[86:89], v[126:133], v[34:41], v[168:171]
	v_mfma_f32_16x16x128_f8f6f4 v[82:85], v[138:145], v[34:41], v[172:175]
	v_mfma_f32_16x16x128_f8f6f4 v[70:73], v[126:133], v[42:49], v[176:179]
	v_mfma_f32_16x16x128_f8f6f4 v[66:69], v[138:145], v[42:49], v[180:183]
	s_setprio 0
	s_mov_b32 m0, s47
	s_barrier
	ds_read_b128 v[26:29], v154 offset:49152
	ds_read_b128 v[30:33], v154 offset:50176
	ds_read_b128 v[34:37], v154 offset:51200
	ds_read_b128 v[38:41], v154 offset:52224
	ds_read_b128 v[160:163], v154 offset:53248
	ds_read_b128 v[164:167], v154 offset:54272
	ds_read_b128 v[168:171], v154 offset:55296
	ds_read_b128 v[172:175], v154 offset:56320
	buffer_load_dwordx4 v1, s[20:23], s68 offen lds
	s_mov_b32 m0, s48
	s_nop 0
	buffer_load_dwordx4 v252, s[20:23], s68 offen lds
	s_barrier
	s_setprio 1
	s_waitcnt lgkmcnt(6)
	v_mfma_f32_16x16x128_f8f6f4 v[62:65], v[2:9], v[26:33], v[62:65]
	v_mfma_f32_16x16x128_f8f6f4 v[58:61], v[10:17], v[26:33], v[58:61]
	s_waitcnt lgkmcnt(4)
	v_mfma_f32_16x16x128_f8f6f4 v[46:49], v[2:9], v[34:41], v[184:187]
	v_mfma_f32_16x16x128_f8f6f4 v[42:45], v[10:17], v[34:41], v[188:191]
	s_waitcnt lgkmcnt(2)
	v_mfma_f32_16x16x128_f8f6f4 v[22:25], v[2:9], v[160:167], v[216:219]
	v_mfma_f32_16x16x128_f8f6f4 v[18:21], v[10:17], v[160:167], v[220:223]
	s_waitcnt lgkmcnt(0)
	v_mfma_f32_16x16x128_f8f6f4 v[6:9], v[2:9], v[168:175], v[224:227]
	v_mfma_f32_16x16x128_f8f6f4 v[2:5], v[10:17], v[168:175], v[228:231]
	s_setprio 0
	s_barrier
	s_add_i32 s67, s67, 0x40080
	s_mov_b32 m0, s49
	s_nop 0
	buffer_load_dwordx4 v253, s[24:27], s67 offen lds
	s_mov_b32 m0, s50
	s_nop 0
	buffer_load_dwordx4 v150, s[24:27], s67 offen lds
	s_waitcnt vmcnt(6)
	s_barrier
; #define LAS __attribute__((address_space(3)))
;     __device__ __forceinline__ void operator()(const f32x4 (&acc)[2][2][4][2], const Unit& u, int wr, int wc, int fr, int fq, LAS const unsigned char* tbl, LAS const unsigned char* b2l) const {
;     ...
;         for (int bj = 0; bj < 2; ++bj)
; #pragma unroll
;             for (int n = 0; n < 2; ++n) bv[bj][n] = *(LAS const f32x4*)(b2l + (wc * 32 + 8 * fq + bj * HALF + 4 * n) * 4);
; #pragma unroll
;         for (int ai = 0; ai < 2; ++ai)
; #pragma unroll
;             for (int m = 0; m < 4; ++m) { const int row = r0 + ai * HALF + m * 16;
;                 if (u.pos0 + row < u.cnt) { const int pid = *(LAS const int*)(tbl + row * 4); const float gt = *(LAS const float*)(tbl + 1024 + row * 4) * Y_FP8_SCALE; unsigned char* rowp = Y + (size_t)pid * D_ + col0;
; #pragma unroll
;                     for (int bj = 0; bj < 2; ++bj) { const f32x4 v0 = (acc[ai][bj][m][0] * (1.0f / W_FP8_SCALE) + bv[bj][0]) * gt, v1 = (acc[ai][bj][m][1] * (1.0f / W_FP8_SCALE) + bv[bj][1]) * gt;
;                         u32x2 w; w.x = pk4_fp8(v0[0], v0[1], v0[2], v0[3]); w.y = pk4_fp8(v1[0], v1[1], v1[2], v1[3]);
;                         *(u32x2*)(rowp + bj * HALF) = w; } } }
;     ...
;         if (FP8 == 2) { for (int t = 0; t < 8; t += 2) PG8_ITER(false); for (int t = 8; t < nt; t += 2) PG8_ITER(true); }
;         else { for (int t = 0; t < nt; t += 2) PG8_ITER(FP8 == 1); }
	s_setprio 1
	v_mfma_f32_16x16x128_f8f6f4 v[54:57], v[126:133], v[26:33], v[54:57]
	v_mfma_f32_16x16x128_f8f6f4 v[50:53], v[138:145], v[26:33], v[50:53]
	v_mfma_f32_16x16x128_f8f6f4 v[30:33], v[126:133], v[34:41], v[232:235]
	v_mfma_f32_16x16x128_f8f6f4 v[26:29], v[138:145], v[34:41], v[236:239]
	v_mfma_f32_16x16x128_f8f6f4 v[38:41], v[126:133], v[160:167], v[240:243]
	v_mfma_f32_16x16x128_f8f6f4 v[34:37], v[138:145], v[160:167], v[244:247]
	v_mfma_f32_16x16x128_f8f6f4 v[14:17], v[126:133], v[168:175], v[248:251]
	v_mfma_f32_16x16x128_f8f6f4 v[10:13], v[138:145], v[168:175], v[146:149]
	s_setprio 0
	s_add_i32 s66, s66, 2
	s_addk_i32 s1, 0x100
	s_addk_i32 s19, 0x100
	s_cmp_gt_u32 s66, 13
	s_barrier
	s_cbranch_scc0 .LBB0_1081
	s_lshl_b32 s0, s65, 11
	s_add_i32 s18, s0, 0
	s_lshl_b32 s0, s65, 10
	s_add_i32 s18, s18, 0x20000
	s_add_i32 s0, s0, 0x21800
	v_mov_b32_e32 v146, v0
	s_cmp_lt_i32 s65, 2
	s_cselect_b32 s0, s0, 0x23800
	v_lshrrev_b32_e32 v126, 1, v146
	v_and_b32_e32 v147, 24, v126
	s_add_i32 s0, s0, 0
	v_or_b32_e32 v126, s44, v147
	v_lshl_add_u32 v126, v126, 2, s0
	ds_read_b128 v[142:145], v126
	ds_read_b128 v[138:141], v126 offset:16
	ds_read_b128 v[130:133], v126 offset:512
	ds_read_b128 v[126:129], v126 offset:528
	s_lshl_b32 s0, s64, 8
	s_or_b32 s0, s0, s44
	v_and_or_b32 v159, v146, 15, s43
	v_or_b32_e32 v146, s0, v147
	v_ashrrev_i32_e32 v147, 31, v146
	v_add_u32_e32 v148, s34, v159
	v_lshl_add_u64 v[146:147], s[6:7], 0, v[146:147]
	v_cmp_gt_i32_e32 vcc, s33, v148
	s_and_saveexec_b64 s[0:1], vcc
	s_cbranch_execz .LBB0_1084
	v_lshl_add_u32 v148, v159, 2, s18
	ds_read2st64_b32 v[148:149], v148 offset1:4
	s_waitcnt lgkmcnt(4)
	v_pk_fma_f32 v[134:135], v[134:135], s[28:29], v[142:143] op_sel_hi:[1,0,1]
	v_pk_fma_f32 v[136:137], v[136:137], s[28:29], v[144:145] op_sel_hi:[1,0,1]
	s_waitcnt lgkmcnt(3)
	v_pk_fma_f32 v[124:125], v[124:125], s[28:29], v[140:141] op_sel_hi:[1,0,1]
	v_pk_fma_f32 v[122:123], v[122:123], s[28:29], v[138:139] op_sel_hi:[1,0,1]
	s_waitcnt lgkmcnt(0)
	v_ashrrev_i32_e32 v161, 31, v148
	v_mov_b32_e32 v160, v148
	v_mul_f32_e32 v148, 0x41800000, v149
	v_pk_mul_f32 v[134:135], v[134:135], v[148:149] op_sel_hi:[1,0]
	v_pk_mul_f32 v[136:137], v[136:137], v[148:149] op_sel_hi:[1,0]
	v_pk_mul_f32 v[124:125], v[124:125], v[148:149] op_sel_hi:[1,0]
	v_pk_mul_f32 v[122:123], v[122:123], v[148:149] op_sel_hi:[1,0]
	v_med3_f32 v149, v134, s55, v158
	v_med3_f32 v135, v135, s55, v158
	v_cvt_pk_fp8_f32 v134, v149, v135
	v_med3_f32 v122, v122, s55, v158
	v_med3_f32 v123, v123, s55, v158
	v_cvt_pk_fp8_f32 v135, v122, v123
	v_pk_fma_f32 v[118:119], v[118:119], s[28:29], v[130:131] op_sel_hi:[1,0,1]
	v_med3_f32 v122, v124, s55, v158
	v_med3_f32 v123, v125, s55, v158
	v_pk_mul_f32 v[118:119], v[118:119], v[148:149] op_sel_hi:[1,0]
	v_pk_fma_f32 v[114:115], v[114:115], s[28:29], v[126:127] op_sel_hi:[1,0,1]
	v_cvt_pk_fp8_f32 v135, v122, v123 op_sel:[0,0,1]
	v_pk_mul_f32 v[114:115], v[114:115], v[148:149] op_sel_hi:[1,0]
	v_med3_f32 v122, v118, s55, v158
	v_med3_f32 v119, v119, s55, v158
	v_cvt_pk_fp8_f32 v118, v122, v119
	v_med3_f32 v114, v114, s55, v158
	v_med3_f32 v115, v115, s55, v158
	v_cvt_pk_fp8_f32 v119, v114, v115
	v_pk_fma_f32 v[120:121], v[120:121], s[28:29], v[132:133] op_sel_hi:[1,0,1]
	v_pk_fma_f32 v[116:117], v[116:117], s[28:29], v[128:129] op_sel_hi:[1,0,1]
	v_med3_f32 v136, v136, s55, v158
	v_med3_f32 v137, v137, s55, v158
	v_pk_mul_f32 v[120:121], v[120:121], v[148:149] op_sel_hi:[1,0]
	v_pk_mul_f32 v[116:117], v[116:117], v[148:149] op_sel_hi:[1,0]
	v_cvt_pk_fp8_f32 v134, v136, v137 op_sel:[0,0,1]
	v_med3_f32 v120, v120, s55, v158
	v_med3_f32 v121, v121, s55, v158
	v_med3_f32 v114, v116, s55, v158
	v_med3_f32 v115, v117, s55, v158
	v_cvt_pk_fp8_f32 v118, v120, v121 op_sel:[0,0,1]
	v_cvt_pk_fp8_f32 v119, v114, v115 op_sel:[0,0,1]
	v_lshlrev_b64 v[114:115], 11, v[160:161]
	v_lshl_add_u64 v[114:115], v[146:147], 0, v[114:115]
	global_store_dwordx2 v[114:115], v[134:135], off
	global_store_dwordx2 v[114:115], v[118:119], off offset:128
